# K2 and K3 result stores made write-through (sc0 sc1) on top of v050
# baseline (speedup 1.0000x reference)
.LBB1_2:
	s_or_b64 exec, exec, s[6:7]
	v_cmp_eq_u32_e32 vcc, 0, v0
	s_waitcnt lgkmcnt(0)
	s_barrier
	s_and_saveexec_b64 s[4:5], vcc
	s_cbranch_execz .LBB1_4
	v_mov_b32_e32 v10, 0
	ds_read_b128 v[0:3], v10
	s_mov_b64 s[4:5], s[28:29]
	s_mov_b64 s[6:7], s[30:31]
	s_mov_b64 s[8:9], s[32:33]
	s_mov_b32 s0, 0
	s_mov_b32 s1, 0x40df4000
	s_mov_b32 s3, 0
	s_waitcnt lgkmcnt(0)
	v_cmp_lt_f64_e32 vcc, v[2:3], v[0:1]
	ds_read_b64 v[8:9], v10 offset:32
	ds_read_b128 v[4:7], v10 offset:16
	v_cndmask_b32_e32 v1, v1, v3, vcc
	v_cndmask_b32_e32 v0, v0, v2, vcc
	v_add_f64 v[0:1], v[0:1], s[0:1]
	s_lshl_b64 s[0:1], s[2:3], 3
	s_add_u32 s4, s4, s0
	s_addc_u32 s5, s5, s1
	s_lshl_b64 s[2:3], s[2:3], 2
	s_add_u32 s2, s6, s2
	s_addc_u32 s3, s7, s3
	s_add_u32 s0, s8, s0
	s_waitcnt lgkmcnt(1)
	v_cndmask_b32_e32 v2, v8, v9, vcc
	global_store_dwordx2 v10, v[0:1], s[4:5] sc0 sc1
	s_waitcnt lgkmcnt(0)
	v_add_f64 v[0:1], v[4:5], v[6:7]
	s_addc_u32 s1, s9, s1
	global_store_dword v10, v2, s[2:3] sc0 sc1
	global_store_dwordx2 v10, v[0:1], s[0:1] sc0 sc1

.LBB2_13:
	s_or_b64 exec, exec, s[10:11]
	s_waitcnt vmcnt(0)
	v_mov_b32_dpp v8, v2 quad_perm:[1,0,3,2] row_mask:0xf bank_mask:0xf bound_ctrl:1
	v_mov_b32_dpp v9, v3 quad_perm:[1,0,3,2] row_mask:0xf bank_mask:0xf bound_ctrl:1
	v_add_f64 v[2:3], v[2:3], v[8:9]
	v_and_b32_e32 v11, 7, v0
	s_add_i32 s3, s2, 0xfffffe00
	v_mov_b32_dpp v8, v2 quad_perm:[2,3,0,1] row_mask:0xf bank_mask:0xf bound_ctrl:1
	v_mov_b32_dpp v9, v3 quad_perm:[2,3,0,1] row_mask:0xf bank_mask:0xf bound_ctrl:1
	v_add_f64 v[2:3], v[2:3], v[8:9]
	v_cmp_eq_u32_e32 vcc, 0, v11
	s_nop 0
	v_mov_b32_dpp v8, v2 row_half_mirror row_mask:0xf bank_mask:0xf bound_ctrl:1
	v_mov_b32_dpp v9, v3 row_half_mirror row_mask:0xf bank_mask:0xf bound_ctrl:1
	s_and_saveexec_b64 s[10:11], vcc
	s_cbranch_execz .LBB2_16
	v_cndmask_b32_e64 v1, v1, v10, s[12:13]
	v_lshrrev_b32_e32 v10, 1, v0
	s_cmp_lg_u32 s3, 0
	ds_write_b32 v10, v1
	s_cbranch_scc1 .LBB2_16
	v_cndmask_b32_e64 v5, v5, v7, s[12:13]
	v_cndmask_b32_e64 v4, v4, v6, s[12:13]
	v_add_f64 v[2:3], v[2:3], v[8:9]
	v_add_f64 v[2:3], v[4:5], v[2:3]
	s_mov_b32 s12, 0
	v_max_f64 v[2:3], v[2:3], 0
	s_brev_b32 s13, 8
	v_mov_b32_e32 v5, 0x100
	v_cmp_gt_f64_e32 vcc, s[12:13], v[2:3]
	v_cvt_f32_i32_e32 v1, v1
	v_lshrrev_b32_e32 v10, 3, v0
	v_cndmask_b32_e32 v5, 0, v5, vcc
	v_ldexp_f64 v[2:3], v[2:3], v5
	v_rsq_f64_e32 v[6:7], v[2:3]
	v_lshlrev_b32_e32 v4, 2, v10
	v_mov_b32_e32 v5, 0
	v_lshl_add_u64 v[8:9], s[8:9], 0, v[4:5]
	global_store_dword v4, v1, s[8:9] sc0 sc1
	v_mul_f64 v[4:5], v[2:3], v[6:7]
	v_mul_f64 v[6:7], v[6:7], 0.5
	v_fma_f64 v[10:11], -v[6:7], v[4:5], 0.5
	v_fmac_f64_e32 v[4:5], v[4:5], v[10:11]
	v_fma_f64 v[12:13], -v[4:5], v[4:5], v[2:3]
	v_fmac_f64_e32 v[6:7], v[6:7], v[10:11]
	v_fmac_f64_e32 v[4:5], v[12:13], v[6:7]
	v_fma_f64 v[10:11], -v[4:5], v[4:5], v[2:3]
	v_mov_b32_e32 v1, 0xffffff80
	v_fmac_f64_e32 v[4:5], v[10:11], v[6:7]
	v_cndmask_b32_e32 v1, 0, v1, vcc
	v_ldexp_f64 v[4:5], v[4:5], v1
	v_mov_b32_e32 v1, 0x260
	v_cmp_class_f64_e32 vcc, v[2:3], v1
	s_nop 1
	v_cndmask_b32_e32 v3, v5, v3, vcc
	v_cndmask_b32_e32 v2, v4, v2, vcc
	v_cvt_f32_f64_e32 v1, v[2:3]
	v_add_co_u32_e32 v2, vcc, 0x3e8000, v8
	s_nop 1
	v_addc_co_u32_e32 v3, vcc, 0, v9, vcc
	global_store_dword v[2:3], v1, off offset:128 sc0 sc1
.LBB2_16:
	s_or_b64 exec, exec, s[10:11]
	s_movk_i32 s10, 0x80
	v_cmp_gt_u32_e32 vcc, s10, v0
	s_waitcnt lgkmcnt(0)
	s_barrier
	s_and_saveexec_b64 s[10:11], vcc
	s_cbranch_execz .LBB2_18
	v_mov_b32_e32 v1, 0
	ds_read_b128 v[2:5], v1
	v_lshl_or_b32 v18, s3, 7, v0
	ds_read_b128 v[6:9], v1 offset:16
	ds_read_b128 v[10:13], v1 offset:32
	ds_read_b128 v[14:17], v1 offset:48
	v_ashrrev_i32_e32 v19, 31, v18
	s_waitcnt lgkmcnt(0)
	v_cmp_eq_u32_e32 vcc, v2, v18
	v_lshlrev_b64 v[20:21], 2, v[18:19]
	s_nop 0
	v_cndmask_b32_e64 v2, 0, 1.0, vcc
	v_cmp_eq_u32_e32 vcc, v3, v18
	s_nop 1
	v_cndmask_b32_e64 v3, 0, 1.0, vcc
	v_cmp_eq_u32_e32 vcc, v4, v18
	v_add_f32_e32 v2, v2, v3
	s_nop 0
	v_cndmask_b32_e64 v3, 0, 1.0, vcc
	v_cmp_eq_u32_e32 vcc, v5, v18
	v_add_f32_e32 v2, v2, v3
	s_nop 0
	v_cndmask_b32_e64 v3, 0, 1.0, vcc
	v_cmp_eq_u32_e32 vcc, v6, v18
	v_add_f32_e32 v2, v2, v3
	s_nop 0
	v_cndmask_b32_e64 v3, 0, 1.0, vcc
	v_cmp_eq_u32_e32 vcc, v7, v18
	v_add_f32_e32 v2, v2, v3
	s_nop 0
	v_cndmask_b32_e64 v3, 0, 1.0, vcc
	v_cmp_eq_u32_e32 vcc, v8, v18
	v_add_f32_e32 v2, v2, v3
	s_nop 0
	v_cndmask_b32_e64 v3, 0, 1.0, vcc
	v_add_f32_e32 v4, v2, v3
	v_cmp_eq_u32_e32 vcc, v9, v18
	s_nop 1
	v_cndmask_b32_e64 v2, 0, 1.0, vcc
	v_cmp_eq_u32_e32 vcc, v10, v18
	v_add_f32_e32 v2, v4, v2
	s_nop 0
	v_cndmask_b32_e64 v3, 0, 1.0, vcc
	v_cmp_eq_u32_e32 vcc, v11, v18
	v_add_f32_e32 v2, v2, v3
	s_nop 0
	v_cndmask_b32_e64 v3, 0, 1.0, vcc
	v_cmp_eq_u32_e32 vcc, v12, v18
	v_add_f32_e32 v2, v2, v3
	s_nop 0
	v_cndmask_b32_e64 v3, 0, 1.0, vcc
	v_cmp_eq_u32_e32 vcc, v13, v18
	v_add_f32_e32 v2, v2, v3
	s_nop 0
	v_cndmask_b32_e64 v3, 0, 1.0, vcc
	v_cmp_eq_u32_e32 vcc, v14, v18
	v_add_f32_e32 v2, v2, v3
	s_nop 0
	v_cndmask_b32_e64 v3, 0, 1.0, vcc
	v_cmp_eq_u32_e32 vcc, v15, v18
	v_add_f32_e32 v2, v2, v3
	s_nop 0
	v_cndmask_b32_e64 v3, 0, 1.0, vcc
	v_cmp_eq_u32_e32 vcc, v16, v18
	v_add_f32_e32 v2, v2, v3
	s_nop 0
	v_cndmask_b32_e64 v3, 0, 1.0, vcc
	v_add_f32_e32 v6, v2, v3
	ds_read_b128 v[2:5], v1 offset:64
	v_cmp_eq_u32_e32 vcc, v17, v18
	s_nop 1
	v_cndmask_b32_e64 v7, 0, 1.0, vcc
	v_add_f32_e32 v10, v6, v7
	ds_read_b128 v[6:9], v1 offset:80
	s_waitcnt lgkmcnt(1)
	v_cmp_eq_u32_e32 vcc, v2, v18
	s_nop 1
	v_cndmask_b32_e64 v2, 0, 1.0, vcc
	v_cmp_eq_u32_e32 vcc, v3, v18
	v_add_f32_e32 v2, v10, v2
	s_nop 0
	v_cndmask_b32_e64 v3, 0, 1.0, vcc
	v_cmp_eq_u32_e32 vcc, v4, v18
	v_add_f32_e32 v2, v2, v3
	s_nop 0
	v_cndmask_b32_e64 v3, 0, 1.0, vcc
	v_cmp_eq_u32_e32 vcc, v5, v18
	v_add_f32_e32 v2, v2, v3
	s_nop 0
	v_cndmask_b32_e64 v3, 0, 1.0, vcc
	s_waitcnt lgkmcnt(0)
	v_cmp_eq_u32_e32 vcc, v6, v18
	v_add_f32_e32 v2, v2, v3
	s_nop 0
	v_cndmask_b32_e64 v3, 0, 1.0, vcc
	v_cmp_eq_u32_e32 vcc, v7, v18
	v_add_f32_e32 v2, v2, v3
	s_nop 0
	v_cndmask_b32_e64 v3, 0, 1.0, vcc
	v_cmp_eq_u32_e32 vcc, v8, v18
	v_add_f32_e32 v2, v2, v3
	s_nop 0
	v_cndmask_b32_e64 v3, 0, 1.0, vcc
	v_add_f32_e32 v6, v2, v3
	ds_read_b128 v[2:5], v1 offset:96
	v_cmp_eq_u32_e32 vcc, v9, v18
	s_nop 1
	v_cndmask_b32_e64 v7, 0, 1.0, vcc
	v_add_f32_e32 v10, v6, v7
	ds_read_b128 v[6:9], v1 offset:112
	s_waitcnt lgkmcnt(1)
	v_cmp_eq_u32_e32 vcc, v2, v18
	s_nop 1
	v_cndmask_b32_e64 v1, 0, 1.0, vcc
	v_cmp_eq_u32_e32 vcc, v3, v18
	v_add_f32_e32 v1, v10, v1
	s_nop 0
	v_cndmask_b32_e64 v2, 0, 1.0, vcc
	v_cmp_eq_u32_e32 vcc, v4, v18
	v_add_f32_e32 v1, v1, v2
	s_nop 0
	v_cndmask_b32_e64 v2, 0, 1.0, vcc
	v_cmp_eq_u32_e32 vcc, v5, v18
	v_add_f32_e32 v1, v1, v2
	s_nop 0
	v_cndmask_b32_e64 v2, 0, 1.0, vcc
	s_waitcnt lgkmcnt(0)
	v_cmp_eq_u32_e32 vcc, v6, v18
	v_add_f32_e32 v1, v1, v2
	s_nop 0
	v_cndmask_b32_e64 v2, 0, 1.0, vcc
	v_cmp_eq_u32_e32 vcc, v7, v18
	v_add_f32_e32 v1, v1, v2
	s_nop 0
	v_cndmask_b32_e64 v2, 0, 1.0, vcc
	v_cmp_eq_u32_e32 vcc, v8, v18
	v_add_f32_e32 v1, v1, v2
	s_nop 0
	v_cndmask_b32_e64 v2, 0, 1.0, vcc
	v_cmp_eq_u32_e32 vcc, v9, v18
	v_add_f32_e32 v1, v1, v2
	s_nop 0
	v_cndmask_b32_e64 v2, 0, 1.0, vcc
	v_add_f32_e32 v1, v1, v2
	v_lshl_add_u64 v[2:3], s[8:9], 0, v[20:21]
	v_add_co_u32_e32 v2, vcc, 0x3e8000, v2
	s_waitcnt vmcnt(0)
	v_add_f32_e32 v1, v1, v23
	v_addc_co_u32_e32 v3, vcc, 0, v3, vcc
	global_store_dword v[2:3], v1, off offset:256 sc0 sc1

.LBB2_32:
	s_or_b64 exec, exec, s[4:5]
	s_mul_i32 s3, s3, 0x1f400
	v_readfirstlane_b32 s4, v6
	s_and_b32 s2, s2, 15
	s_mul_i32 s6, s2, 0x1f40
	s_add_u32 s2, s8, s3
	s_addc_u32 s3, s9, 0
	s_add_u32 s2, s2, s6
	s_addc_u32 s3, s3, 0
	s_mul_hi_i32 s5, s4, 0x1f400
	s_mul_i32 s4, s4, 0x1f400
	s_add_u32 s4, s4, s6
	s_addc_u32 s5, s5, 0
	s_add_u32 s0, s18, s4
	s_addc_u32 s1, s19, s5
	v_lshlrev_b32_e32 v2, 4, v0
	v_cmp_gt_u32_e32 vcc, 0xf4, v0
	global_load_dwordx4 v[6:9], v2, s[0:1] nt
	s_add_u32 s0, s0, 0x1000
	s_addc_u32 s1, s1, 0
	s_and_saveexec_b64 s[6:7], vcc
	global_load_dwordx4 v[10:13], v2, s[0:1] nt
	s_mov_b64 exec, s[6:7]
	s_waitcnt vmcnt(1)
	global_store_dwordx4 v2, v[6:9], s[2:3] offset:128 sc0 sc1
	s_add_u32 s2, s2, 0x1000
	s_addc_u32 s3, s3, 0
	s_and_b64 exec, exec, vcc
	s_waitcnt vmcnt(1)
	global_store_dwordx4 v2, v[10:13], s[2:3] offset:128 sc0 sc1
